# speedup vs baseline: 1.1138x; 1.0101x over previous
_Z11center_prepPKfPcPfS2_:
	s_load_dwordx2 s[6:7], s[0:1], 0x0
	s_load_dwordx4 s[8:11], s[0:1], 0x8
	s_load_dwordx2 s[12:13], s[0:1], 0x18
	v_lshrrev_b32_e32 v1, 3, v0
	v_and_b32_e32 v2, 7, v0
	v_lshlrev_b32_e32 v3, 10, v1
	v_lshl_or_b32 v136, v2, 4, v3
	v_mul_u32_u24_e32 v3, 0x110, v1
	v_lshl_add_u32 v137, v2, 4, v3
	v_and_b32_e32 v4, 31, v0
	v_lshrrev_b32_e32 v5, 5, v0
	v_mul_u32_u24_e32 v3, 0x110, v4
	v_lshl_add_u32 v138, v5, 5, v3
	v_lshlrev_b32_e32 v139, 5, v0
	v_lshlrev_b32_e32 v140, 2, v1
	v_mov_b32_e32 v142, -2.0
	v_mov_b32_e32 v143, -2.0
	s_lshl_b32 s14, s2, 15
	s_waitcnt lgkmcnt(0)
	s_add_u32 s16, s6, s14
	s_addc_u32 s17, s7, 0
	global_load_dwordx4 v[8:11], v136, s[16:17] offset:0 nt
	global_load_dwordx4 v[12:15], v136, s[16:17] offset:128 nt
	global_load_dwordx4 v[16:19], v136, s[16:17] offset:256 nt
	global_load_dwordx4 v[20:23], v136, s[16:17] offset:384 nt
	global_load_dwordx4 v[24:27], v136, s[16:17] offset:512 nt
	global_load_dwordx4 v[28:31], v136, s[16:17] offset:640 nt
	global_load_dwordx4 v[32:35], v136, s[16:17] offset:768 nt
	global_load_dwordx4 v[36:39], v136, s[16:17] offset:896 nt
	s_add_u32 s18, s16, 0x2000
	s_addc_u32 s19, s17, 0
	global_load_dwordx4 v[40:43], v136, s[18:19] offset:0 nt
	global_load_dwordx4 v[44:47], v136, s[18:19] offset:128 nt
	global_load_dwordx4 v[48:51], v136, s[18:19] offset:256 nt
	global_load_dwordx4 v[52:55], v136, s[18:19] offset:384 nt
	global_load_dwordx4 v[56:59], v136, s[18:19] offset:512 nt
	global_load_dwordx4 v[60:63], v136, s[18:19] offset:640 nt
	global_load_dwordx4 v[64:67], v136, s[18:19] offset:768 nt
	global_load_dwordx4 v[68:71], v136, s[18:19] offset:896 nt
	s_add_u32 s20, s16, 0x4000
	s_addc_u32 s21, s17, 0
	global_load_dwordx4 v[72:75], v136, s[20:21] offset:0 nt
	global_load_dwordx4 v[76:79], v136, s[20:21] offset:128 nt
	global_load_dwordx4 v[80:83], v136, s[20:21] offset:256 nt
	global_load_dwordx4 v[84:87], v136, s[20:21] offset:384 nt
	global_load_dwordx4 v[88:91], v136, s[20:21] offset:512 nt
	global_load_dwordx4 v[92:95], v136, s[20:21] offset:640 nt
	global_load_dwordx4 v[96:99], v136, s[20:21] offset:768 nt
	global_load_dwordx4 v[100:103], v136, s[20:21] offset:896 nt
	s_add_u32 s22, s16, 0x6000
	s_addc_u32 s23, s17, 0
	global_load_dwordx4 v[104:107], v136, s[22:23] offset:0 nt
	global_load_dwordx4 v[108:111], v136, s[22:23] offset:128 nt
	global_load_dwordx4 v[112:115], v136, s[22:23] offset:256 nt
	global_load_dwordx4 v[116:119], v136, s[22:23] offset:384 nt
	global_load_dwordx4 v[120:123], v136, s[22:23] offset:512 nt
	global_load_dwordx4 v[124:127], v136, s[22:23] offset:640 nt
	global_load_dwordx4 v[128:131], v136, s[22:23] offset:768 nt
	global_load_dwordx4 v[132:135], v136, s[22:23] offset:896 nt
	s_lshl_b32 s14, s2, 13
	s_add_u32 s24, s8, s14
	s_addc_u32 s25, s9, 0
	s_add_u32 s26, s24, 0x1000
	s_addc_u32 s27, s25, 0
	s_lshl_b32 s14, s2, 7
	s_add_u32 s28, s10, s14
	s_addc_u32 s29, s11, 0
	s_cmp_lg_u32 s2, 0
	s_cbranch_scc1 .Lprep_noinit
	v_cmp_gt_u32_e32 vcc, 16, v0
	s_and_saveexec_b64 s[30:31], vcc
	v_lshlrev_b32_e32 v1, 7, v0
	v_add_u32_e32 v1, 0x300000, v1
	v_mov_b32_e32 v2, 0
	v_mov_b32_e32 v3, 0
	global_store_dwordx2 v1, v[2:3], s[8:9]
	v_cmp_eq_u32_e32 vcc, 0, v0
	s_and_b64 exec, exec, vcc
	global_store_dword v2, v2, s[12:13]
	s_or_b64 exec, exec, s[30:31]

_Z11center_mainPKfPKcS0_Pf:
	s_load_dwordx4 s[4:7], s[0:1], 0x0
	s_load_dwordx2 s[8:9], s[0:1], 0x10
	s_and_b32 s3, s2, 7
	s_lshr_b32 s12, s2, 3
	s_mov_b32 s30, s2
	v_lshrrev_b32_e32 v1, 6, v0
	v_and_b32_e32 v2, 63, v0
	v_bfe_u32 v3, v0, 3, 3
	v_and_b32_e32 v4, 7, v0
	v_lshrrev_b32_e32 v5, 7, v0
	v_bfe_u32 v6, v0, 6, 1
	v_lshl_or_b32 v7, v5, 3, v3
	v_lshlrev_b32_e32 v8, 10, v7
	v_lshl_or_b32 v8, v6, 9, v8
	v_lshl_or_b32 v226, v4, 4, v8
	v_lshlrev_b32_e32 v17, 15, v1
	v_lshl_or_b32 v227, v2, 5, v17
	v_lshlrev_b32_e32 v237, 3, v0
	s_lshl_b32 s13, s3, 22
	s_lshl_b32 s14, s12, 15
	s_add_u32 s13, s13, s14
	s_lshl_b32 s15, s3, 18
	s_lshl_b32 s28, s3, 12
	s_waitcnt lgkmcnt(0)
	s_add_u32 s16, s4, s13
	s_addc_u32 s17, s5, 0
	global_load_dwordx4 v[194:197], v226, s[16:17] offset:0 nt
	global_load_dwordx4 v[198:201], v226, s[16:17] offset:128 nt
	global_load_dwordx4 v[202:205], v226, s[16:17] offset:256 nt
	global_load_dwordx4 v[206:209], v226, s[16:17] offset:384 nt
	s_add_u32 s8, s8, s28
	s_addc_u32 s9, s9, 0
	global_load_dwordx2 v[238:239], v237, s[8:9]
	s_add_u32 s24, s6, s15
	s_addc_u32 s25, s7, 0
	s_add_u32 s32, s24, 0x1000
	s_addc_u32 s33, s25, 0
	s_add_u32 s34, s24, 0x2000
	s_addc_u32 s35, s25, 0
	s_add_u32 s36, s24, 0x3000
	s_addc_u32 s37, s25, 0
	s_add_u32 s38, s24, 0x4000
	s_addc_u32 s39, s25, 0
	s_add_u32 s40, s24, 0x5000
	s_addc_u32 s41, s25, 0
	s_add_u32 s42, s24, 0x6000
	s_addc_u32 s43, s25, 0
	s_add_u32 s44, s24, 0x7000
	s_addc_u32 s45, s25, 0
	global_load_dwordx4 v[34:37], v227, s[24:25] offset:0
	global_load_dwordx4 v[38:41], v227, s[24:25] offset:16
	global_load_dwordx4 v[26:29], v227, s[24:25] offset:2048
	global_load_dwordx4 v[30:33], v227, s[24:25] offset:2064
	global_load_dwordx4 v[50:53], v227, s[32:33] offset:0
	global_load_dwordx4 v[54:57], v227, s[32:33] offset:16
	global_load_dwordx4 v[42:45], v227, s[32:33] offset:2048
	global_load_dwordx4 v[46:49], v227, s[32:33] offset:2064
	global_load_dwordx4 v[18:21], v227, s[34:35] offset:0
	global_load_dwordx4 v[22:25], v227, s[34:35] offset:16
	global_load_dwordx4 v[130:133], v227, s[34:35] offset:2048
	global_load_dwordx4 v[134:137], v227, s[34:35] offset:2064
	global_load_dwordx4 v[122:125], v227, s[36:37] offset:0
	global_load_dwordx4 v[126:129], v227, s[36:37] offset:16
	global_load_dwordx4 v[138:141], v227, s[36:37] offset:2048
	global_load_dwordx4 v[142:145], v227, s[36:37] offset:2064
	global_load_dwordx4 v[98:101], v227, s[38:39] offset:0
	global_load_dwordx4 v[102:105], v227, s[38:39] offset:16
	global_load_dwordx4 v[90:93], v227, s[38:39] offset:2048
	global_load_dwordx4 v[94:97], v227, s[38:39] offset:2064
	global_load_dwordx4 v[114:117], v227, s[40:41] offset:0
	global_load_dwordx4 v[118:121], v227, s[40:41] offset:16
	global_load_dwordx4 v[106:109], v227, s[40:41] offset:2048
	global_load_dwordx4 v[110:113], v227, s[40:41] offset:2064
	global_load_dwordx4 v[58:61], v227, s[42:43] offset:0
	global_load_dwordx4 v[62:65], v227, s[42:43] offset:16
	global_load_dwordx4 v[66:69], v227, s[42:43] offset:2048
	global_load_dwordx4 v[70:73], v227, s[42:43] offset:2064
	global_load_dwordx4 v[74:77], v227, s[44:45] offset:0
	global_load_dwordx4 v[78:81], v227, s[44:45] offset:16
	global_load_dwordx4 v[82:85], v227, s[44:45] offset:2048
	global_load_dwordx4 v[86:89], v227, s[44:45] offset:2064
	s_add_u32 s18, s16, 0x100000
	s_addc_u32 s19, s17, 0
	s_add_u32 s20, s16, 0x200000
	s_addc_u32 s21, s17, 0
	s_add_u32 s22, s16, 0x300000
	s_addc_u32 s23, s17, 0
	v_mul_u32_u24_e32 v9, 0x110, v7
	v_lshl_add_u32 v9, v6, 7, v9
	v_lshl_add_u32 v228, v4, 4, v9
	v_lshlrev_b32_e32 v10, 6, v7
	v_lshl_or_b32 v10, v6, 5, v10
	v_lshl_or_b32 v229, v4, 2, v10
	v_and_b32_e32 v11, 31, v0
	v_bfe_u32 v12, v0, 5, 1
	v_mul_u32_u24_e32 v13, 0x110, v11
	v_lshl_add_u32 v230, v12, 5, v13
	v_lshlrev_b32_e32 v14, 9, v1
	v_lshl_or_b32 v231, v12, 4, v14
	v_xor_b32_e32 v15, 32, v2
	v_lshlrev_b32_e32 v232, 2, v15
	v_xor_b32_e32 v15, 16, v2
	v_lshlrev_b32_e32 v247, 2, v15
	v_lshlrev_b32_e32 v16, 7, v1
	v_lshl_or_b32 v233, v11, 2, v16
	v_mov_b32_e32 v234, 0x7f7f7f7f
	s_waitcnt vmcnt(32)
	ds_write_b64 v237, v[238:239] offset:34816
	v_mul_f32_e32 v244, v194, v194
	v_mul_f32_e32 v245, v198, v198
	v_cvt_pk_fp8_f32 v240, v194, v195
	v_cvt_pk_fp8_f32 v241, v198, v199
	v_cvt_pk_fp8_f32 v242, v202, v203
	v_cvt_pk_fp8_f32 v243, v206, v207
	v_fmac_f32_e32 v244, v195, v195
	v_fmac_f32_e32 v245, v199, v199
	v_fmac_f32_e32 v244, v196, v196
	v_fmac_f32_e32 v245, v200, v200
	v_fmac_f32_e32 v244, v197, v197
	v_fmac_f32_e32 v245, v201, v201
	v_fmac_f32_e32 v244, v202, v202
	v_fmac_f32_e32 v245, v206, v206
	v_fmac_f32_e32 v244, v203, v203
	v_fmac_f32_e32 v245, v207, v207
	v_fmac_f32_e32 v244, v204, v204
	v_fmac_f32_e32 v245, v208, v208
	v_fmac_f32_e32 v244, v205, v205
	v_fmac_f32_e32 v245, v209, v209
	v_cvt_pk_fp8_f32 v240, v196, v197 op_sel:[0,0,1]
	v_cvt_pk_fp8_f32 v241, v200, v201 op_sel:[0,0,1]
	v_cvt_pk_fp8_f32 v242, v204, v205 op_sel:[0,0,1]
	v_cvt_pk_fp8_f32 v243, v208, v209 op_sel:[0,0,1]
	v_add_f32_e32 v244, v244, v245
	s_nop 0
	ds_write_b128 v228, v[240:243] offset:0
	ds_write_b32 v229, v244 offset:38912
	global_load_dwordx4 v[210:213], v226, s[18:19] offset:0 nt
	global_load_dwordx4 v[214:217], v226, s[18:19] offset:128 nt
	global_load_dwordx4 v[218:221], v226, s[18:19] offset:256 nt
	global_load_dwordx4 v[222:225], v226, s[18:19] offset:384 nt
	s_waitcnt lgkmcnt(0)
	s_barrier
	ds_read_b128 v[162:165], v230 offset:0
	ds_read_b128 v[166:169], v230 offset:16
	ds_read_b128 v[2:5], v231 offset:34816
	ds_read_b128 v[6:9], v231 offset:34848
	ds_read_b128 v[10:13], v231 offset:34880
	ds_read_b128 v[14:17], v231 offset:34912
	ds_read_b128 v[170:173], v230 offset:64
	ds_read_b128 v[174:177], v230 offset:80
	ds_read_b128 v[178:181], v230 offset:128
	ds_read_b128 v[182:185], v230 offset:144
	ds_read_b128 v[186:189], v230 offset:192
	ds_read_b128 v[190:193], v230 offset:208
	s_waitcnt vmcnt(34) lgkmcnt(6)
	v_mfma_scale_f32_32x32x64_f8f6f4 v[2:17], v[34:41], v[162:169], v[2:17], v234, v234 op_sel_hi:[0,0,0]
	s_waitcnt vmcnt(32) lgkmcnt(4)
	v_mfma_scale_f32_32x32x64_f8f6f4 v[2:17], v[26:33], v[170:177], v[2:17], v234, v234 op_sel_hi:[0,0,0]
	s_waitcnt vmcnt(30) lgkmcnt(2)
	v_mfma_scale_f32_32x32x64_f8f6f4 v[2:17], v[50:57], v[178:185], v[2:17], v234, v234 op_sel_hi:[0,0,0]
	s_waitcnt vmcnt(28) lgkmcnt(0)
	v_mfma_scale_f32_32x32x64_f8f6f4 v[2:17], v[42:49], v[186:193], v[2:17], v234, v234 op_sel_hi:[0,0,0]
	ds_read_b128 v[146:149], v231 offset:34944
	ds_read_b128 v[150:153], v231 offset:34976
	ds_read_b128 v[154:157], v231 offset:35008
	ds_read_b128 v[158:161], v231 offset:35040
	s_waitcnt vmcnt(26) lgkmcnt(0)
	v_mfma_scale_f32_32x32x64_f8f6f4 v[146:161], v[18:25], v[162:169], v[146:161], v234, v234 op_sel_hi:[0,0,0]
	s_waitcnt vmcnt(24)
	v_mfma_scale_f32_32x32x64_f8f6f4 v[146:161], v[130:137], v[170:177], v[146:161], v234, v234 op_sel_hi:[0,0,0]
	s_waitcnt vmcnt(22)
	v_mfma_scale_f32_32x32x64_f8f6f4 v[146:161], v[122:129], v[178:185], v[146:161], v234, v234 op_sel_hi:[0,0,0]
	s_waitcnt vmcnt(20)
	v_mfma_scale_f32_32x32x64_f8f6f4 v[146:161], v[138:145], v[186:193], v[146:161], v234, v234 op_sel_hi:[0,0,0]
	s_nop 15
	v_min3_f32 v2, v2, v3, v4
	v_min3_f32 v5, v5, v6, v7
	v_min3_f32 v8, v8, v9, v10
	v_min3_f32 v11, v11, v12, v13
	v_min3_f32 v14, v14, v15, v16
	v_min3_f32 v2, v2, v5, v8
	v_min3_f32 v11, v11, v14, v17
	v_min_f32_e32 v235, v2, v11
	ds_read_b128 v[2:5], v231 offset:35072
	ds_read_b128 v[6:9], v231 offset:35104
	ds_read_b128 v[10:13], v231 offset:35136
	ds_read_b128 v[14:17], v231 offset:35168
	s_waitcnt vmcnt(18) lgkmcnt(0)
	v_mfma_scale_f32_32x32x64_f8f6f4 v[2:17], v[98:105], v[162:169], v[2:17], v234, v234 op_sel_hi:[0,0,0]
	s_waitcnt vmcnt(16)
	v_mfma_scale_f32_32x32x64_f8f6f4 v[2:17], v[90:97], v[170:177], v[2:17], v234, v234 op_sel_hi:[0,0,0]
	s_waitcnt vmcnt(14)
	v_mfma_scale_f32_32x32x64_f8f6f4 v[2:17], v[114:121], v[178:185], v[2:17], v234, v234 op_sel_hi:[0,0,0]
	s_waitcnt vmcnt(12)
	v_mfma_scale_f32_32x32x64_f8f6f4 v[2:17], v[106:113], v[186:193], v[2:17], v234, v234 op_sel_hi:[0,0,0]
	s_nop 15
	v_min3_f32 v146, v146, v147, v148
	v_min3_f32 v149, v149, v150, v151
	v_min3_f32 v152, v152, v153, v154
	v_min3_f32 v155, v155, v156, v157
	v_min3_f32 v158, v158, v159, v160
	v_min3_f32 v146, v146, v149, v152
	v_min3_f32 v155, v155, v158, v161
	v_min3_f32 v235, v235, v146, v155
	ds_read_b128 v[146:149], v231 offset:35200
	ds_read_b128 v[150:153], v231 offset:35232
	ds_read_b128 v[154:157], v231 offset:35264
	ds_read_b128 v[158:161], v231 offset:35296
	s_waitcnt vmcnt(10) lgkmcnt(0)
	v_mfma_scale_f32_32x32x64_f8f6f4 v[146:161], v[58:65], v[162:169], v[146:161], v234, v234 op_sel_hi:[0,0,0]
	s_waitcnt vmcnt(8)
	v_mfma_scale_f32_32x32x64_f8f6f4 v[146:161], v[66:73], v[170:177], v[146:161], v234, v234 op_sel_hi:[0,0,0]
	s_waitcnt vmcnt(6)
	v_mfma_scale_f32_32x32x64_f8f6f4 v[146:161], v[74:81], v[178:185], v[146:161], v234, v234 op_sel_hi:[0,0,0]
	s_waitcnt vmcnt(4)
	v_mfma_scale_f32_32x32x64_f8f6f4 v[146:161], v[82:89], v[186:193], v[146:161], v234, v234 op_sel_hi:[0,0,0]
	s_nop 15
	v_min3_f32 v2, v2, v3, v4
	v_min3_f32 v5, v5, v6, v7
	v_min3_f32 v8, v8, v9, v10
	v_min3_f32 v11, v11, v12, v13
	v_min3_f32 v14, v14, v15, v16
	v_min3_f32 v2, v2, v5, v8
	v_min3_f32 v11, v11, v14, v17
	v_min3_f32 v235, v235, v2, v11
	s_nop 15
	s_nop 3
	v_min3_f32 v146, v146, v147, v148
	v_min3_f32 v149, v149, v150, v151
	v_min3_f32 v152, v152, v153, v154
	v_min3_f32 v155, v155, v156, v157
	v_min3_f32 v158, v158, v159, v160
	v_min3_f32 v146, v146, v149, v152
	v_min3_f32 v155, v155, v158, v161
	v_min3_f32 v235, v235, v146, v155
	ds_bpermute_b32 v246, v232, v235
	s_waitcnt lgkmcnt(0)
	v_min_f32_e32 v246, v235, v246
	ds_write_b32 v233, v246 offset:47104
	global_load_dwordx4 v[194:197], v226, s[20:21] offset:0 nt
	global_load_dwordx4 v[198:201], v226, s[20:21] offset:128 nt
	global_load_dwordx4 v[202:205], v226, s[20:21] offset:256 nt
	global_load_dwordx4 v[206:209], v226, s[20:21] offset:384 nt
	s_waitcnt vmcnt(4)
	v_mul_f32_e32 v244, v210, v210
	v_mul_f32_e32 v245, v214, v214
	v_cvt_pk_fp8_f32 v240, v210, v211
	v_cvt_pk_fp8_f32 v241, v214, v215
	v_cvt_pk_fp8_f32 v242, v218, v219
	v_cvt_pk_fp8_f32 v243, v222, v223
	v_fmac_f32_e32 v244, v211, v211
	v_fmac_f32_e32 v245, v215, v215
	v_fmac_f32_e32 v244, v212, v212
	v_fmac_f32_e32 v245, v216, v216
	v_fmac_f32_e32 v244, v213, v213
	v_fmac_f32_e32 v245, v217, v217
	v_fmac_f32_e32 v244, v218, v218
	v_fmac_f32_e32 v245, v222, v222
	v_fmac_f32_e32 v244, v219, v219
	v_fmac_f32_e32 v245, v223, v223
	v_fmac_f32_e32 v244, v220, v220
	v_fmac_f32_e32 v245, v224, v224
	v_fmac_f32_e32 v244, v221, v221
	v_fmac_f32_e32 v245, v225, v225
	v_cvt_pk_fp8_f32 v240, v212, v213 op_sel:[0,0,1]
	v_cvt_pk_fp8_f32 v241, v216, v217 op_sel:[0,0,1]
	v_cvt_pk_fp8_f32 v242, v220, v221 op_sel:[0,0,1]
	v_cvt_pk_fp8_f32 v243, v224, v225 op_sel:[0,0,1]
	v_add_f32_e32 v244, v244, v245
	s_nop 0
	ds_write_b128 v228, v[240:243] offset:8704
	ds_write_b32 v229, v244 offset:40960
	s_waitcnt lgkmcnt(0)
	s_barrier
	ds_read_b128 v[162:165], v230 offset:8704
	ds_read_b128 v[166:169], v230 offset:8720
	ds_read_b128 v[2:5], v231 offset:34816
	ds_read_b128 v[6:9], v231 offset:34848
	ds_read_b128 v[10:13], v231 offset:34880
	ds_read_b128 v[14:17], v231 offset:34912
	ds_read_b128 v[170:173], v230 offset:8768
	ds_read_b128 v[174:177], v230 offset:8784
	ds_read_b128 v[178:181], v230 offset:8832
	ds_read_b128 v[182:185], v230 offset:8848
	ds_read_b128 v[186:189], v230 offset:8896
	ds_read_b128 v[190:193], v230 offset:8912
	s_waitcnt lgkmcnt(6)
	v_mfma_scale_f32_32x32x64_f8f6f4 v[2:17], v[34:41], v[162:169], v[2:17], v234, v234 op_sel_hi:[0,0,0]
	s_waitcnt lgkmcnt(4)
	v_mfma_scale_f32_32x32x64_f8f6f4 v[2:17], v[26:33], v[170:177], v[2:17], v234, v234 op_sel_hi:[0,0,0]
	s_waitcnt lgkmcnt(2)
	v_mfma_scale_f32_32x32x64_f8f6f4 v[2:17], v[50:57], v[178:185], v[2:17], v234, v234 op_sel_hi:[0,0,0]
	s_waitcnt lgkmcnt(0)
	v_mfma_scale_f32_32x32x64_f8f6f4 v[2:17], v[42:49], v[186:193], v[2:17], v234, v234 op_sel_hi:[0,0,0]
	ds_read_b128 v[146:149], v231 offset:34944
	ds_read_b128 v[150:153], v231 offset:34976
	ds_read_b128 v[154:157], v231 offset:35008
	ds_read_b128 v[158:161], v231 offset:35040
	s_waitcnt lgkmcnt(0)
	v_mfma_scale_f32_32x32x64_f8f6f4 v[146:161], v[18:25], v[162:169], v[146:161], v234, v234 op_sel_hi:[0,0,0]
	v_mfma_scale_f32_32x32x64_f8f6f4 v[146:161], v[130:137], v[170:177], v[146:161], v234, v234 op_sel_hi:[0,0,0]
	v_mfma_scale_f32_32x32x64_f8f6f4 v[146:161], v[122:129], v[178:185], v[146:161], v234, v234 op_sel_hi:[0,0,0]
	v_mfma_scale_f32_32x32x64_f8f6f4 v[146:161], v[138:145], v[186:193], v[146:161], v234, v234 op_sel_hi:[0,0,0]
	s_nop 15
	v_min3_f32 v2, v2, v3, v4
	v_min3_f32 v5, v5, v6, v7
	v_min3_f32 v8, v8, v9, v10
	v_min3_f32 v11, v11, v12, v13
	v_min3_f32 v14, v14, v15, v16
	v_min3_f32 v2, v2, v5, v8
	v_min3_f32 v11, v11, v14, v17
	v_min_f32_e32 v235, v2, v11
	ds_read_b128 v[2:5], v231 offset:35072
	ds_read_b128 v[6:9], v231 offset:35104
	ds_read_b128 v[10:13], v231 offset:35136
	ds_read_b128 v[14:17], v231 offset:35168
	s_waitcnt lgkmcnt(0)
	v_mfma_scale_f32_32x32x64_f8f6f4 v[2:17], v[98:105], v[162:169], v[2:17], v234, v234 op_sel_hi:[0,0,0]
	v_mfma_scale_f32_32x32x64_f8f6f4 v[2:17], v[90:97], v[170:177], v[2:17], v234, v234 op_sel_hi:[0,0,0]
	v_mfma_scale_f32_32x32x64_f8f6f4 v[2:17], v[114:121], v[178:185], v[2:17], v234, v234 op_sel_hi:[0,0,0]
	v_mfma_scale_f32_32x32x64_f8f6f4 v[2:17], v[106:113], v[186:193], v[2:17], v234, v234 op_sel_hi:[0,0,0]
	s_nop 15
	v_min3_f32 v146, v146, v147, v148
	v_min3_f32 v149, v149, v150, v151
	v_min3_f32 v152, v152, v153, v154
	v_min3_f32 v155, v155, v156, v157
	v_min3_f32 v158, v158, v159, v160
	v_min3_f32 v146, v146, v149, v152
	v_min3_f32 v155, v155, v158, v161
	v_min3_f32 v235, v235, v146, v155
	ds_read_b128 v[146:149], v231 offset:35200
	ds_read_b128 v[150:153], v231 offset:35232
	ds_read_b128 v[154:157], v231 offset:35264
	ds_read_b128 v[158:161], v231 offset:35296
	s_waitcnt lgkmcnt(0)
	v_mfma_scale_f32_32x32x64_f8f6f4 v[146:161], v[58:65], v[162:169], v[146:161], v234, v234 op_sel_hi:[0,0,0]
	v_mfma_scale_f32_32x32x64_f8f6f4 v[146:161], v[66:73], v[170:177], v[146:161], v234, v234 op_sel_hi:[0,0,0]
	v_mfma_scale_f32_32x32x64_f8f6f4 v[146:161], v[74:81], v[178:185], v[146:161], v234, v234 op_sel_hi:[0,0,0]
	v_mfma_scale_f32_32x32x64_f8f6f4 v[146:161], v[82:89], v[186:193], v[146:161], v234, v234 op_sel_hi:[0,0,0]
	s_nop 15
	v_min3_f32 v2, v2, v3, v4
	v_min3_f32 v5, v5, v6, v7
	v_min3_f32 v8, v8, v9, v10
	v_min3_f32 v11, v11, v12, v13
	v_min3_f32 v14, v14, v15, v16
	v_min3_f32 v2, v2, v5, v8
	v_min3_f32 v11, v11, v14, v17
	v_min3_f32 v235, v235, v2, v11
	s_nop 15
	s_nop 3
	v_min3_f32 v146, v146, v147, v148
	v_min3_f32 v149, v149, v150, v151
	v_min3_f32 v152, v152, v153, v154
	v_min3_f32 v155, v155, v156, v157
	v_min3_f32 v158, v158, v159, v160
	v_min3_f32 v146, v146, v149, v152
	v_min3_f32 v155, v155, v158, v161
	v_min3_f32 v235, v235, v146, v155
	ds_bpermute_b32 v246, v232, v235
	s_waitcnt lgkmcnt(0)
	v_min_f32_e32 v246, v235, v246
	ds_write_b32 v233, v246 offset:48128
	global_load_dwordx4 v[210:213], v226, s[22:23] offset:0 nt
	global_load_dwordx4 v[214:217], v226, s[22:23] offset:128 nt
	global_load_dwordx4 v[218:221], v226, s[22:23] offset:256 nt
	global_load_dwordx4 v[222:225], v226, s[22:23] offset:384 nt
	s_waitcnt vmcnt(4)
	v_mul_f32_e32 v244, v194, v194
	v_mul_f32_e32 v245, v198, v198
	v_cvt_pk_fp8_f32 v240, v194, v195
	v_cvt_pk_fp8_f32 v241, v198, v199
	v_cvt_pk_fp8_f32 v242, v202, v203
	v_cvt_pk_fp8_f32 v243, v206, v207
	v_fmac_f32_e32 v244, v195, v195
	v_fmac_f32_e32 v245, v199, v199
	v_fmac_f32_e32 v244, v196, v196
	v_fmac_f32_e32 v245, v200, v200
	v_fmac_f32_e32 v244, v197, v197
	v_fmac_f32_e32 v245, v201, v201
	v_fmac_f32_e32 v244, v202, v202
	v_fmac_f32_e32 v245, v206, v206
	v_fmac_f32_e32 v244, v203, v203
	v_fmac_f32_e32 v245, v207, v207
	v_fmac_f32_e32 v244, v204, v204
	v_fmac_f32_e32 v245, v208, v208
	v_fmac_f32_e32 v244, v205, v205
	v_fmac_f32_e32 v245, v209, v209
	v_cvt_pk_fp8_f32 v240, v196, v197 op_sel:[0,0,1]
	v_cvt_pk_fp8_f32 v241, v200, v201 op_sel:[0,0,1]
	v_cvt_pk_fp8_f32 v242, v204, v205 op_sel:[0,0,1]
	v_cvt_pk_fp8_f32 v243, v208, v209 op_sel:[0,0,1]
	v_add_f32_e32 v244, v244, v245
	s_nop 0
	ds_write_b128 v228, v[240:243] offset:17408
	ds_write_b32 v229, v244 offset:43008
	s_waitcnt lgkmcnt(0)
	s_barrier
	ds_read_b128 v[162:165], v230 offset:17408
	ds_read_b128 v[166:169], v230 offset:17424
	ds_read_b128 v[2:5], v231 offset:34816
	ds_read_b128 v[6:9], v231 offset:34848
	ds_read_b128 v[10:13], v231 offset:34880
	ds_read_b128 v[14:17], v231 offset:34912
	ds_read_b128 v[170:173], v230 offset:17472
	ds_read_b128 v[174:177], v230 offset:17488
	ds_read_b128 v[178:181], v230 offset:17536
	ds_read_b128 v[182:185], v230 offset:17552
	ds_read_b128 v[186:189], v230 offset:17600
	ds_read_b128 v[190:193], v230 offset:17616
	s_waitcnt lgkmcnt(6)
	v_mfma_scale_f32_32x32x64_f8f6f4 v[2:17], v[34:41], v[162:169], v[2:17], v234, v234 op_sel_hi:[0,0,0]
	s_waitcnt lgkmcnt(4)
	v_mfma_scale_f32_32x32x64_f8f6f4 v[2:17], v[26:33], v[170:177], v[2:17], v234, v234 op_sel_hi:[0,0,0]
	s_waitcnt lgkmcnt(2)
	v_mfma_scale_f32_32x32x64_f8f6f4 v[2:17], v[50:57], v[178:185], v[2:17], v234, v234 op_sel_hi:[0,0,0]
	s_waitcnt lgkmcnt(0)
	v_mfma_scale_f32_32x32x64_f8f6f4 v[2:17], v[42:49], v[186:193], v[2:17], v234, v234 op_sel_hi:[0,0,0]
	ds_read_b128 v[146:149], v231 offset:34944
	ds_read_b128 v[150:153], v231 offset:34976
	ds_read_b128 v[154:157], v231 offset:35008
	ds_read_b128 v[158:161], v231 offset:35040
	s_waitcnt lgkmcnt(0)
	v_mfma_scale_f32_32x32x64_f8f6f4 v[146:161], v[18:25], v[162:169], v[146:161], v234, v234 op_sel_hi:[0,0,0]
	v_mfma_scale_f32_32x32x64_f8f6f4 v[146:161], v[130:137], v[170:177], v[146:161], v234, v234 op_sel_hi:[0,0,0]
	v_mfma_scale_f32_32x32x64_f8f6f4 v[146:161], v[122:129], v[178:185], v[146:161], v234, v234 op_sel_hi:[0,0,0]
	v_mfma_scale_f32_32x32x64_f8f6f4 v[146:161], v[138:145], v[186:193], v[146:161], v234, v234 op_sel_hi:[0,0,0]
	s_nop 15
	v_min3_f32 v2, v2, v3, v4
	v_min3_f32 v5, v5, v6, v7
	v_min3_f32 v8, v8, v9, v10
	v_min3_f32 v11, v11, v12, v13
	v_min3_f32 v14, v14, v15, v16
	v_min3_f32 v2, v2, v5, v8
	v_min3_f32 v11, v11, v14, v17
	v_min_f32_e32 v235, v2, v11
	ds_read_b128 v[2:5], v231 offset:35072
	ds_read_b128 v[6:9], v231 offset:35104
	ds_read_b128 v[10:13], v231 offset:35136
	ds_read_b128 v[14:17], v231 offset:35168
	s_waitcnt lgkmcnt(0)
	v_mfma_scale_f32_32x32x64_f8f6f4 v[2:17], v[98:105], v[162:169], v[2:17], v234, v234 op_sel_hi:[0,0,0]
	v_mfma_scale_f32_32x32x64_f8f6f4 v[2:17], v[90:97], v[170:177], v[2:17], v234, v234 op_sel_hi:[0,0,0]
	v_mfma_scale_f32_32x32x64_f8f6f4 v[2:17], v[114:121], v[178:185], v[2:17], v234, v234 op_sel_hi:[0,0,0]
	v_mfma_scale_f32_32x32x64_f8f6f4 v[2:17], v[106:113], v[186:193], v[2:17], v234, v234 op_sel_hi:[0,0,0]
	s_nop 15
	v_min3_f32 v146, v146, v147, v148
	v_min3_f32 v149, v149, v150, v151
	v_min3_f32 v152, v152, v153, v154
	v_min3_f32 v155, v155, v156, v157
	v_min3_f32 v158, v158, v159, v160
	v_min3_f32 v146, v146, v149, v152
	v_min3_f32 v155, v155, v158, v161
	v_min3_f32 v235, v235, v146, v155
	ds_read_b128 v[146:149], v231 offset:35200
	ds_read_b128 v[150:153], v231 offset:35232
	ds_read_b128 v[154:157], v231 offset:35264
	ds_read_b128 v[158:161], v231 offset:35296
	s_waitcnt lgkmcnt(0)
	v_mfma_scale_f32_32x32x64_f8f6f4 v[146:161], v[58:65], v[162:169], v[146:161], v234, v234 op_sel_hi:[0,0,0]
	v_mfma_scale_f32_32x32x64_f8f6f4 v[146:161], v[66:73], v[170:177], v[146:161], v234, v234 op_sel_hi:[0,0,0]
	v_mfma_scale_f32_32x32x64_f8f6f4 v[146:161], v[74:81], v[178:185], v[146:161], v234, v234 op_sel_hi:[0,0,0]
	v_mfma_scale_f32_32x32x64_f8f6f4 v[146:161], v[82:89], v[186:193], v[146:161], v234, v234 op_sel_hi:[0,0,0]
	s_nop 15
	v_min3_f32 v2, v2, v3, v4
	v_min3_f32 v5, v5, v6, v7
	v_min3_f32 v8, v8, v9, v10
	v_min3_f32 v11, v11, v12, v13
	v_min3_f32 v14, v14, v15, v16
	v_min3_f32 v2, v2, v5, v8
	v_min3_f32 v11, v11, v14, v17
	v_min3_f32 v235, v235, v2, v11
	s_nop 15
	s_nop 3
	v_min3_f32 v146, v146, v147, v148
	v_min3_f32 v149, v149, v150, v151
	v_min3_f32 v152, v152, v153, v154
	v_min3_f32 v155, v155, v156, v157
	v_min3_f32 v158, v158, v159, v160
	v_min3_f32 v146, v146, v149, v152
	v_min3_f32 v155, v155, v158, v161
	v_min3_f32 v235, v235, v146, v155
	ds_bpermute_b32 v246, v232, v235
	s_waitcnt lgkmcnt(0)
	v_min_f32_e32 v246, v235, v246
	ds_write_b32 v233, v246 offset:49152
	s_waitcnt vmcnt(0)
	v_mul_f32_e32 v244, v210, v210
	v_mul_f32_e32 v245, v214, v214
	v_cvt_pk_fp8_f32 v240, v210, v211
	v_cvt_pk_fp8_f32 v241, v214, v215
	v_cvt_pk_fp8_f32 v242, v218, v219
	v_cvt_pk_fp8_f32 v243, v222, v223
	v_fmac_f32_e32 v244, v211, v211
	v_fmac_f32_e32 v245, v215, v215
	v_fmac_f32_e32 v244, v212, v212
	v_fmac_f32_e32 v245, v216, v216
	v_fmac_f32_e32 v244, v213, v213
	v_fmac_f32_e32 v245, v217, v217
	v_fmac_f32_e32 v244, v218, v218
	v_fmac_f32_e32 v245, v222, v222
	v_fmac_f32_e32 v244, v219, v219
	v_fmac_f32_e32 v245, v223, v223
	v_fmac_f32_e32 v244, v220, v220
	v_fmac_f32_e32 v245, v224, v224
	v_fmac_f32_e32 v244, v221, v221
	v_fmac_f32_e32 v245, v225, v225
	v_cvt_pk_fp8_f32 v240, v212, v213 op_sel:[0,0,1]
	v_cvt_pk_fp8_f32 v241, v216, v217 op_sel:[0,0,1]
	v_cvt_pk_fp8_f32 v242, v220, v221 op_sel:[0,0,1]
	v_cvt_pk_fp8_f32 v243, v224, v225 op_sel:[0,0,1]
	v_add_f32_e32 v244, v244, v245
	s_nop 0
	ds_write_b128 v228, v[240:243] offset:26112
	ds_write_b32 v229, v244 offset:45056
	s_waitcnt lgkmcnt(0)
	s_barrier
	ds_read_b128 v[162:165], v230 offset:26112
	ds_read_b128 v[166:169], v230 offset:26128
	ds_read_b128 v[2:5], v231 offset:34816
	ds_read_b128 v[6:9], v231 offset:34848
	ds_read_b128 v[10:13], v231 offset:34880
	ds_read_b128 v[14:17], v231 offset:34912
	ds_read_b128 v[170:173], v230 offset:26176
	ds_read_b128 v[174:177], v230 offset:26192
	ds_read_b128 v[178:181], v230 offset:26240
	ds_read_b128 v[182:185], v230 offset:26256
	ds_read_b128 v[186:189], v230 offset:26304
	ds_read_b128 v[190:193], v230 offset:26320
	s_waitcnt lgkmcnt(6)
	v_mfma_scale_f32_32x32x64_f8f6f4 v[2:17], v[34:41], v[162:169], v[2:17], v234, v234 op_sel_hi:[0,0,0]
	s_waitcnt lgkmcnt(4)
	v_mfma_scale_f32_32x32x64_f8f6f4 v[2:17], v[26:33], v[170:177], v[2:17], v234, v234 op_sel_hi:[0,0,0]
	s_waitcnt lgkmcnt(2)
	v_mfma_scale_f32_32x32x64_f8f6f4 v[2:17], v[50:57], v[178:185], v[2:17], v234, v234 op_sel_hi:[0,0,0]
	s_waitcnt lgkmcnt(0)
	v_mfma_scale_f32_32x32x64_f8f6f4 v[2:17], v[42:49], v[186:193], v[2:17], v234, v234 op_sel_hi:[0,0,0]
	ds_read_b128 v[146:149], v231 offset:34944
	ds_read_b128 v[150:153], v231 offset:34976
	ds_read_b128 v[154:157], v231 offset:35008
	ds_read_b128 v[158:161], v231 offset:35040
	s_waitcnt lgkmcnt(0)
	v_mfma_scale_f32_32x32x64_f8f6f4 v[146:161], v[18:25], v[162:169], v[146:161], v234, v234 op_sel_hi:[0,0,0]
	v_mfma_scale_f32_32x32x64_f8f6f4 v[146:161], v[130:137], v[170:177], v[146:161], v234, v234 op_sel_hi:[0,0,0]
	v_mfma_scale_f32_32x32x64_f8f6f4 v[146:161], v[122:129], v[178:185], v[146:161], v234, v234 op_sel_hi:[0,0,0]
	v_mfma_scale_f32_32x32x64_f8f6f4 v[146:161], v[138:145], v[186:193], v[146:161], v234, v234 op_sel_hi:[0,0,0]
	s_nop 15
	v_min3_f32 v2, v2, v3, v4
	v_min3_f32 v5, v5, v6, v7
	v_min3_f32 v8, v8, v9, v10
	v_min3_f32 v11, v11, v12, v13
	v_min3_f32 v14, v14, v15, v16
	v_min3_f32 v2, v2, v5, v8
	v_min3_f32 v11, v11, v14, v17
	v_min_f32_e32 v235, v2, v11
	ds_read_b128 v[2:5], v231 offset:35072
	ds_read_b128 v[6:9], v231 offset:35104
	ds_read_b128 v[10:13], v231 offset:35136
	ds_read_b128 v[14:17], v231 offset:35168
	s_waitcnt lgkmcnt(0)
	v_mfma_scale_f32_32x32x64_f8f6f4 v[2:17], v[98:105], v[162:169], v[2:17], v234, v234 op_sel_hi:[0,0,0]
	v_mfma_scale_f32_32x32x64_f8f6f4 v[2:17], v[90:97], v[170:177], v[2:17], v234, v234 op_sel_hi:[0,0,0]
	v_mfma_scale_f32_32x32x64_f8f6f4 v[2:17], v[114:121], v[178:185], v[2:17], v234, v234 op_sel_hi:[0,0,0]
	v_mfma_scale_f32_32x32x64_f8f6f4 v[2:17], v[106:113], v[186:193], v[2:17], v234, v234 op_sel_hi:[0,0,0]
	s_nop 15
	v_min3_f32 v146, v146, v147, v148
	v_min3_f32 v149, v149, v150, v151
	v_min3_f32 v152, v152, v153, v154
	v_min3_f32 v155, v155, v156, v157
	v_min3_f32 v158, v158, v159, v160
	v_min3_f32 v146, v146, v149, v152
	v_min3_f32 v155, v155, v158, v161
	v_min3_f32 v235, v235, v146, v155
	ds_read_b128 v[146:149], v231 offset:35200
	ds_read_b128 v[150:153], v231 offset:35232
	ds_read_b128 v[154:157], v231 offset:35264
	ds_read_b128 v[158:161], v231 offset:35296
	s_waitcnt lgkmcnt(0)
	v_mfma_scale_f32_32x32x64_f8f6f4 v[146:161], v[58:65], v[162:169], v[146:161], v234, v234 op_sel_hi:[0,0,0]
	v_mfma_scale_f32_32x32x64_f8f6f4 v[146:161], v[66:73], v[170:177], v[146:161], v234, v234 op_sel_hi:[0,0,0]
	v_mfma_scale_f32_32x32x64_f8f6f4 v[146:161], v[74:81], v[178:185], v[146:161], v234, v234 op_sel_hi:[0,0,0]
	v_mfma_scale_f32_32x32x64_f8f6f4 v[146:161], v[82:89], v[186:193], v[146:161], v234, v234 op_sel_hi:[0,0,0]
	s_nop 15
	v_min3_f32 v2, v2, v3, v4
	v_min3_f32 v5, v5, v6, v7
	v_min3_f32 v8, v8, v9, v10
	v_min3_f32 v11, v11, v12, v13
	v_min3_f32 v14, v14, v15, v16
	v_min3_f32 v2, v2, v5, v8
	v_min3_f32 v11, v11, v14, v17
	v_min3_f32 v235, v235, v2, v11
	s_nop 15
	s_nop 3
	v_min3_f32 v146, v146, v147, v148
	v_min3_f32 v149, v149, v150, v151
	v_min3_f32 v152, v152, v153, v154
	v_min3_f32 v155, v155, v156, v157
	v_min3_f32 v158, v158, v159, v160
	v_min3_f32 v146, v146, v149, v152
	v_min3_f32 v155, v155, v158, v161
	v_min3_f32 v235, v235, v146, v155
	ds_bpermute_b32 v246, v232, v235
	s_waitcnt lgkmcnt(0)
	v_min_f32_e32 v246, v235, v246
	ds_write_b32 v233, v246 offset:50176
	s_waitcnt lgkmcnt(0)
	s_barrier
	v_readfirstlane_b32 s2, v1
	s_nop 3
	s_cmp_gt_u32 s2, 1
	s_cbranch_scc1 .Lmain_idle
	v_and_b32_e32 v2, 31, v0
	v_lshlrev_b32_e32 v3, 5, v0
	v_and_b32_e32 v3, 0xc00, v3
	v_lshl_or_b32 v8, v2, 2, v3
	v_add_u32_e32 v8, 0xb800, v8
	v_lshlrev_b32_e32 v14, 6, v0
	ds_read2_b32 v[2:3], v8 offset1:32
	ds_read2_b32 v[4:5], v8 offset0:64 offset1:96
	ds_read2_b32 v[6:7], v8 offset0:128 offset1:160
	ds_read2_b32 v[10:11], v8 offset0:192 offset1:224
	ds_read_b128 v[20:23], v14 offset:38912
	ds_read_b128 v[24:27], v14 offset:38928
	ds_read_b128 v[28:31], v14 offset:38944
	ds_read_b128 v[32:35], v14 offset:38960
	s_mov_b32 s8, 0xf800000
	s_waitcnt lgkmcnt(4)
	v_min3_f32 v2, v2, v3, v4
	v_min3_f32 v5, v5, v6, v7
	v_min3_f32 v2, v2, v10, v11
	v_min_f32_e32 v2, v2, v5
	s_waitcnt lgkmcnt(0)
	v_add_f32_e32 v20, v20, v21
	v_add_f32_e32 v22, v22, v23
	v_add_f32_e32 v24, v24, v25
	v_add_f32_e32 v26, v26, v27
	v_add_f32_e32 v28, v28, v29
	v_add_f32_e32 v30, v30, v31
	v_add_f32_e32 v32, v32, v33
	v_add_f32_e32 v34, v34, v35
	v_add_f32_e32 v20, v20, v22
	v_add_f32_e32 v24, v24, v26
	v_add_f32_e32 v28, v28, v30
	v_add_f32_e32 v32, v32, v34
	v_add_f32_e32 v20, v20, v24
	v_add_f32_e32 v28, v28, v32
	v_add_f32_e32 v20, v20, v28
	v_add_f32_e32 v2, v2, v20
	v_max_f32_e32 v2, 0, v2
	v_mul_f32_e32 v3, 0x4f800000, v2
	v_cmp_gt_f32_e32 vcc, s8, v2
	s_nop 1
	v_cndmask_b32_e32 v2, v2, v3, vcc
	v_sqrt_f32_e32 v3, v2
	s_nop 0
	v_add_u32_e32 v4, -1, v3
	v_fma_f32 v5, -v4, v3, v2
	v_cmp_ge_f32_e64 s[10:11], 0, v5
	v_add_u32_e32 v5, 1, v3
	s_nop 0
	v_cndmask_b32_e64 v4, v3, v4, s[10:11]
	v_fma_f32 v3, -v5, v3, v2
	v_cmp_lt_f32_e64 s[10:11], 0, v3
	s_nop 1
	v_cndmask_b32_e64 v3, v4, v5, s[10:11]
	v_mul_f32_e32 v4, 0x37800000, v3
	v_cndmask_b32_e32 v3, v3, v4, vcc
	v_mov_b32_e32 v4, 0x260
	v_cmp_class_f32_e32 vcc, v2, v4
	s_nop 1
	v_cndmask_b32_e32 v2, v3, v2, vcc
	s_nop 1
	v_add_f32_dpp v3, v2, v2 quad_perm:[1,0,3,2] row_mask:0xf bank_mask:0xf
	s_nop 1
	v_add_f32_dpp v4, v3, v3 quad_perm:[2,3,0,1] row_mask:0xf bank_mask:0xf
	s_nop 1
	v_add_f32_dpp v5, v4, v4 row_half_mirror row_mask:0xf bank_mask:0xf
	s_nop 1
	v_add_f32_dpp v6, v5, v5 row_mirror row_mask:0xf bank_mask:0xf
	s_nop 1
	v_readlane_b32 s12, v6, 0
	v_readlane_b32 s13, v6, 16
	v_readlane_b32 s14, v6, 32
	v_readlane_b32 s15, v6, 48
	s_nop 3
	v_mov_b32_e32 v7, s12
	v_add_f32_e32 v7, s13, v7
	v_mov_b32_e32 v9, s14
	v_add_f32_e32 v9, s15, v9
	v_add_f32_e32 v7, v7, v9
	v_mov_b32_e32 v4, 0
	s_cmp_eq_u32 s2, 1
	s_cbranch_scc0 .Lmain_w0
	ds_write_b32 v4, v7 offset:51204
	s_waitcnt lgkmcnt(0)
